# U phase: wave 7 also stages its packed words (slots 0-95) in the LDS left below the control block; one flush path for all eight waves
# speedup vs baseline: 1.0049x; 1.0049x over previous
; template <int VAR> __device__ __forceinline__ void u_process_grp(const UGrp& d, const v4u (&xb)[16], int j, size_t t0, int lane, LAS unsigned char* wl, const unsigned char* __restrict__ UT, const float* __restrict__ egate, unsigned* __restrict__ PW) {
;     ...
;         dv *= __uint_as_float((ent >> 24) << 23) * 0.125f;
;         const pg8::f32x2 gl = pg8::gelu_pk((pg8::f32x2){dv, dv});
;         const float wv = gl.x * gate;
;         if (VAR != 3 && pl < n) PW[(blk * 128 + slot) * 64 + tk0 + tkk] = (__float_as_uint(wv) & 0xFFFE0000u) | ((ent & 0x3FFFu) << 3);
; template <int VAR> __device__ __forceinline__ void peer_u_phase(int wave, int grp, int gwl  , LAS unsigned char* lds, gu32* qhead  , const unsigned char* __restrict__ X1Q, const unsigned char* __restrict__ UT, ...
;     ...
;             for (int r = 0; r < 8; ++r) {
;                 const int j = ((h == 0 ? r : 7 - r) + grp) & 7;
;                 if (h == 0) u_process_grp<VAR>(da, xb, j, t0, lane, wl, UT, egate, PW); else u_process_grp<VAR>(db, xb, j, t0 + 4, lane, wl, UT, egate, PW);
;             }
.LBB0_669:
	s_mov_b64 s[34:35], exec
	s_mov_b64 exec, -1
	s_cmp_lg_u64 s[44:45], 0
	s_cselect_b32 s98, s20, s18
	s_cselect_b32 s99, s21, s19
	v_mbcnt_lo_u32_b32 v124, -1, 0
	v_mbcnt_hi_u32_b32 v124, -1, v124
	v_mov_b32_e32 v126, s61
	v_lshlrev_b32_e32 v125, 4, v124
	v_lshl_add_u32 v125, v126, 11, v125
	v_add_u32_e32 v125, 0x24000, v125
	ds_read_b128 v[56:59], v125
	v_or_b32_e32 v120, s27, v124
	v_mov_b32_e32 v121, s15
	v_lshlrev_b64 v[120:121], 8, v[120:121]
	v_lshl_add_u64 v[120:121], s[98:99], 0, v[120:121]
	s_mov_b64 s[98:99], 0x4000
	v_lshl_add_u64 v[122:123], v[120:121], 0, s[98:99]
	s_cmp_eq_u32 s61, 7
	s_cbranch_scc0 .Lpwf_all_0
	s_mov_b32 exec_hi, 0
.Lpwf_all_0:
	ds_read_b128 v[60:63], v125 offset:1024
	s_waitcnt lgkmcnt(0)
	global_store_dwordx4 v[122:123], v[60:63], off
	s_mov_b64 exec, -1
	global_store_dwordx4 v[120:121], v[56:59], off
	s_mov_b64 exec, s[34:35]

; template <int VAR> __device__ __forceinline__ void u_process_grp(const UGrp& d, const v4u (&xb)[16], int j, size_t t0, int lane, LAS unsigned char* wl, const unsigned char* __restrict__ UT, const float* __restrict__ egate, unsigned* __restrict__ PW) {
;     ...
;         if (VAR != 3 && pl < n) PW[(blk * 128 + slot) * 64 + tk0 + tkk] = (__float_as_uint(wv) & 0xFFFE0000u) | ((ent & 0x3FFFu) << 3);
.Lpwd_0:
	v_cmp_gt_u32_e32 vcc, 0x60, v97
	s_mov_b64 s[98:99], exec
	s_mov_b64 exec, vcc
	v_and_b32_e32 v96, 12, v140
	v_lshl_add_u32 v96, v97, 4, v96
	v_add_u32_e32 v96, 0x27800, v96
	ds_write_b32 v96, v98
	s_andn2_b64 exec, s[98:99], vcc
	v_or_b32_e32 v96, s27, v97
	v_mov_b32_e32 v97, s15
	v_lshlrev_b64 v[96:97], 8, v[96:97]
	v_lshl_add_u64 v[96:97], s[18:19], 0, v[96:97]
	v_lshl_add_u64 v[96:97], v[96:97], 0, v[140:141]
	global_store_dword v[96:97], v98, off
	s_branch .LBB0_707

; template <int VAR> __device__ __forceinline__ void u_process_grp(const UGrp& d, const v4u (&xb)[16], int j, size_t t0, int lane, LAS unsigned char* wl, const unsigned char* __restrict__ UT, const float* __restrict__ egate, unsigned* __restrict__ PW) {
;     ...
;         if (VAR != 3 && pl < n) PW[(blk * 128 + slot) * 64 + tk0 + tkk] = (__float_as_uint(wv) & 0xFFFE0000u) | ((ent & 0x3FFFu) << 3);
.Lpwd_1:
	v_cmp_gt_u32_e32 vcc, 0x60, v97
	s_mov_b64 s[98:99], exec
	s_mov_b64 exec, vcc
	v_and_b32_e32 v96, 12, v140
	v_lshl_add_u32 v96, v97, 4, v96
	v_add_u32_e32 v96, 0x27800, v96
	ds_write_b32 v96, v98
	s_andn2_b64 exec, s[98:99], vcc
	v_or_b32_e32 v96, s27, v97
	v_mov_b32_e32 v97, s15
	v_lshlrev_b64 v[96:97], 8, v[96:97]
	v_lshl_add_u64 v[96:97], s[20:21], 0, v[96:97]
	v_lshl_add_u64 v[96:97], v[96:97], 0, v[140:141]
	global_store_dword v[96:97], v98, off
	s_branch .LBB0_787
